# MoBA output stage (both layers): eight gain quads loaded in one batch, single wait, instead of load/vmcnt(0)/store ladder
# baseline (speedup 1.0000x reference)
.LBB0_788:
	ds_bpermute_b32 v1, v207, v226
	s_mov_b32 s0, 0xf800000
	s_mov_b32 s60, 1
	s_mov_b64 s[28:29], 0
	s_waitcnt lgkmcnt(0)
	v_add_f32_e32 v1, v226, v1
	ds_bpermute_b32 v2, v208, v1
	s_waitcnt lgkmcnt(0)
	v_add_f32_e32 v1, v1, v2
	v_div_scale_f32 v2, s[4:5], v1, v1, 1.0
	v_rcp_f32_e32 v3, v2
	v_div_scale_f32 v4, vcc, 1.0, v1, 1.0
	v_fma_f32 v5, -v2, v3, 1.0
	v_fmac_f32_e32 v3, v5, v3
	v_mul_f32_e32 v5, v4, v3
	v_fma_f32 v6, -v2, v5, v4
	v_fmac_f32_e32 v5, v6, v3
	v_fma_f32 v2, -v2, v5, v4
	v_div_fmas_f32 v2, v2, v3, v5
	v_div_fixup_f32 v6, v2, v1, 1.0
	v_pk_mul_f32 v[10:11], v[80:81], v[6:7] op_sel_hi:[1,0]
	v_pk_mul_f32 v[14:15], v[76:77], v[6:7] op_sel_hi:[1,0]
	v_mov_b32_e32 v4, v11
	v_mov_b32_e32 v5, v15
	v_pk_mul_f32 v[8:9], v[82:83], v[6:7] op_sel_hi:[1,0]
	v_pk_mul_f32 v[12:13], v[78:79], v[6:7] op_sel_hi:[1,0]
	v_mov_b32_e32 v2, v10
	v_mov_b32_e32 v3, v14
	v_pk_mul_f32 v[4:5], v[4:5], v[4:5]
	v_mov_b32_e32 v16, v8
	v_pk_fma_f32 v[2:3], v[2:3], v[2:3], v[4:5]
	v_mov_b32_e32 v4, v9
	v_mov_b32_e32 v5, v13
	v_mov_b32_e32 v17, v12
	v_pk_mul_f32 v[4:5], v[4:5], v[4:5]
	v_pk_mul_f32 v[18:19], v[74:75], v[6:7] op_sel_hi:[1,0]
	v_pk_fma_f32 v[4:5], v[16:17], v[16:17], v[4:5]
	v_pk_mul_f32 v[16:17], v[72:73], v[6:7] op_sel_hi:[1,0]
	v_pk_add_f32 v[2:3], v[2:3], v[4:5]
	v_pk_mul_f32 v[4:5], v[18:19], v[18:19]
	s_waitcnt vmcnt(3)
	v_pk_mul_f32 v[28:29], v[16:17], v[16:17]
	v_pk_add_f32 v[2:3], v[2:3], v[2:3] op_sel_hi:[0,1]
	v_pk_mov_b32 v[30:31], v[28:29], v[4:5] op_sel:[1,0]
	v_mov_b32_e32 v29, v5
	v_pk_add_f32 v[4:5], v[30:31], v[28:29]
	v_pk_mul_f32 v[30:31], v[68:69], v[6:7] op_sel_hi:[1,0]
	v_pk_mul_f32 v[28:29], v[70:71], v[6:7] op_sel_hi:[1,0]
	v_mul_f32_e32 v2, v30, v30
	s_waitcnt vmcnt(2)
	v_pk_fma_f32 v[36:37], v[30:31], v[30:31], v[2:3] op_sel_hi:[1,1,0]
	v_mul_f32_e32 v2, v28, v28
	v_pk_add_f32 v[4:5], v[4:5], v[4:5] op_sel_hi:[0,1]
	v_pk_fma_f32 v[38:39], v[28:29], v[28:29], v[2:3] op_sel_hi:[1,1,0]
	v_pk_mul_f32 v[40:41], v[66:67], v[6:7] op_sel_hi:[1,0]
	v_pk_mul_f32 v[42:43], v[64:65], v[6:7] op_sel_hi:[1,0]
	v_mul_f32_e32 v4, v40, v40
	v_mul_f32_e32 v36, v42, v42
	v_mul_f32_e32 v38, v43, v43
	v_mul_f32_e32 v2, v41, v41
	v_pk_add_f32 v[36:37], v[36:37], v[38:39]
	v_pk_add_f32 v[2:3], v[4:5], v[2:3]
	v_pk_mul_f32 v[32:33], v[32:33], v[6:7] op_sel_hi:[1,0]
	v_pk_add_f32 v[36:37], v[36:37], v[2:3]
	global_load_dwordx4 v[48:51], v[106:107], off
	global_load_dwordx4 v[52:55], v[106:107], off offset:64
	global_load_dwordx4 v[56:59], v[106:107], off offset:128
	global_load_dwordx4 v[60:63], v[106:107], off offset:192
	global_load_dwordx4 v[84:87], v[106:107], off offset:256
	global_load_dwordx4 v[88:91], v[106:107], off offset:320
	global_load_dwordx4 v[92:95], v[106:107], off offset:384
	global_load_dwordx4 v[96:99], v[106:107], off offset:448
	v_pk_mul_f32 v[34:35], v[34:35], v[6:7] op_sel_hi:[1,0]
	v_pk_add_f32 v[36:37], v[36:37], v[36:37] op_sel_hi:[0,1]
	v_pk_mul_f32 v[38:39], v[34:35], v[34:35]
	s_waitcnt vmcnt(9)
	v_pk_mul_f32 v[44:45], v[32:33], v[32:33]
	v_pk_mul_f32 v[24:25], v[24:25], v[6:7] op_sel_hi:[1,0]
	v_pk_mov_b32 v[46:47], v[44:45], v[38:39] op_sel:[1,0]
	v_mov_b32_e32 v45, v39
	v_pk_mul_f32 v[26:27], v[26:27], v[6:7] op_sel_hi:[1,0]
	v_mul_f32_e32 v36, v24, v24
	v_pk_add_f32 v[38:39], v[46:47], v[44:45]
	v_pk_fma_f32 v[44:45], v[24:25], v[24:25], v[36:37] op_sel_hi:[1,1,0]
	v_mul_f32_e32 v36, v26, v26
	v_pk_add_f32 v[38:39], v[38:39], v[38:39] op_sel_hi:[0,1]
	v_pk_fma_f32 v[46:47], v[26:27], v[26:27], v[36:37] op_sel_hi:[1,1,0]
	v_pk_mul_f32 v[22:23], v[22:23], v[6:7] op_sel_hi:[1,0]
	v_pk_mul_f32 v[6:7], v[20:21], v[6:7] op_sel_hi:[1,0]
	v_mul_f32_e32 v38, v22, v22
	v_mul_f32_e32 v44, v6, v6
	v_mul_f32_e32 v46, v7, v7
	v_mul_f32_e32 v36, v23, v23
	v_pk_add_f32 v[20:21], v[44:45], v[46:47]
	v_pk_add_f32 v[36:37], v[38:39], v[36:37]
	s_nop 0
	v_pk_add_f32 v[20:21], v[20:21], v[36:37]
	s_nop 0
	v_add_f32_e32 v1, v20, v21
	ds_bpermute_b32 v20, v207, v1
	s_waitcnt lgkmcnt(0)
	v_add_f32_e32 v1, v1, v20
	ds_bpermute_b32 v20, v208, v1
	s_waitcnt lgkmcnt(0)
	v_add_f32_e32 v1, v1, v20
	v_fmamk_f32 v1, v1, 0x3c000000, v215
	v_mul_f32_e32 v20, 0x4f800000, v1
	v_cmp_gt_f32_e32 vcc, s0, v1
	s_nop 1
	v_cndmask_b32_e32 v1, v1, v20, vcc
	v_sqrt_f32_e32 v20, v1
	s_nop 0
	v_add_u32_e32 v21, -1, v20
	v_fma_f32 v36, -v21, v20, v1
	v_cmp_ge_f32_e64 s[4:5], 0, v36
	v_add_u32_e32 v36, 1, v20
	s_nop 0
	v_cndmask_b32_e64 v21, v20, v21, s[4:5]
	v_fma_f32 v20, -v36, v20, v1
	v_cmp_lt_f32_e64 s[4:5], 0, v20
	s_nop 1
	v_cndmask_b32_e64 v20, v21, v36, s[4:5]
	v_mul_f32_e32 v21, 0x37800000, v20
	v_cndmask_b32_e32 v20, v20, v21, vcc
	v_cmp_class_f32_e32 vcc, v1, v216
	s_nop 1
	v_cndmask_b32_e32 v1, v20, v1, vcc
	v_div_scale_f32 v20, s[4:5], v1, v1, 1.0
	v_rcp_f32_e32 v21, v20
	s_nop 0
	v_fma_f32 v36, -v20, v21, 1.0
	v_fmac_f32_e32 v21, v36, v21
	v_div_scale_f32 v36, vcc, 1.0, v1, 1.0
	v_mul_f32_e32 v37, v36, v21
	v_fma_f32 v38, -v20, v37, v36
	v_fmac_f32_e32 v37, v38, v21
	v_fma_f32 v20, -v20, v37, v36
	v_div_fmas_f32 v20, v20, v21, v37
	v_lshlrev_b64 v[36:37], 12, v[154:155]
	v_div_fixup_f32 v20, v20, v1, 1.0
	v_lshl_add_u64 v[36:37], s[16:17], 0, v[36:37]
	v_lshl_add_u64 v[36:37], v[36:37], 0, s[12:13]
	v_pk_mul_f32 v[10:11], v[10:11], v[20:21] op_sel_hi:[1,0]
	v_pk_mul_f32 v[8:9], v[8:9], v[20:21] op_sel_hi:[1,0]
	v_lshl_add_u64 v[36:37], v[104:105], 1, v[36:37]
	s_waitcnt vmcnt(0)
	v_pk_mul_f32 v[2:3], v[48:49], v[10:11]
	v_pk_mul_f32 v[4:5], v[50:51], v[8:9]
	v_cvt_pk_bf16_f32 v2, v2, v3
	v_cvt_pk_bf16_f32 v3, v4, v5
	v_add_co_u32_e32 v4, vcc, s52, v36
	v_pk_mul_f32 v[10:11], v[14:15], v[20:21] op_sel_hi:[1,0]
	s_nop 0
	v_addc_co_u32_e32 v5, vcc, 0, v37, vcc
	global_store_dwordx2 v[4:5], v[2:3], off offset:2048
	v_pk_mul_f32 v[12:13], v[12:13], v[20:21] op_sel_hi:[1,0]
	v_lshl_add_u64 v[8:9], v[36:37], 0, s[26:27]
	v_pk_mul_f32 v[6:7], v[6:7], v[20:21] op_sel_hi:[1,0]
	s_and_b64 vcc, exec, s[6:7]
	v_pk_mul_f32 v[2:3], v[52:53], v[10:11]
	v_pk_mul_f32 v[4:5], v[54:55], v[12:13]
	v_cvt_pk_bf16_f32 v2, v2, v3
	v_cvt_pk_bf16_f32 v3, v4, v5
	global_store_dwordx2 v[8:9], v[2:3], off offset:32
	v_pk_mul_f32 v[10:11], v[16:17], v[20:21] op_sel_hi:[1,0]
	v_pk_mul_f32 v[12:13], v[18:19], v[20:21] op_sel_hi:[1,0]
	v_pk_mul_f32 v[2:3], v[56:57], v[10:11]
	v_pk_mul_f32 v[4:5], v[58:59], v[12:13]
	v_cvt_pk_bf16_f32 v2, v2, v3
	v_cvt_pk_bf16_f32 v3, v4, v5
	global_store_dwordx2 v[8:9], v[2:3], off offset:64
	v_pk_mul_f32 v[10:11], v[30:31], v[20:21] op_sel_hi:[1,0]
	v_pk_mul_f32 v[12:13], v[28:29], v[20:21] op_sel_hi:[1,0]
	v_pk_mul_f32 v[2:3], v[60:61], v[10:11]
	v_pk_mul_f32 v[4:5], v[62:63], v[12:13]
	v_cvt_pk_bf16_f32 v2, v2, v3
	v_cvt_pk_bf16_f32 v3, v4, v5
	global_store_dwordx2 v[8:9], v[2:3], off offset:96
	v_pk_mul_f32 v[10:11], v[42:43], v[20:21] op_sel_hi:[1,0]
	v_pk_mul_f32 v[12:13], v[40:41], v[20:21] op_sel_hi:[1,0]
	v_pk_mul_f32 v[2:3], v[84:85], v[10:11]
	v_pk_mul_f32 v[4:5], v[86:87], v[12:13]
	v_cvt_pk_bf16_f32 v2, v2, v3
	v_cvt_pk_bf16_f32 v3, v4, v5
	global_store_dwordx2 v[8:9], v[2:3], off offset:128
	v_pk_mul_f32 v[10:11], v[32:33], v[20:21] op_sel_hi:[1,0]
	v_pk_mul_f32 v[12:13], v[34:35], v[20:21] op_sel_hi:[1,0]
	v_pk_mul_f32 v[2:3], v[88:89], v[10:11]
	v_pk_mul_f32 v[4:5], v[90:91], v[12:13]
	v_cvt_pk_bf16_f32 v2, v2, v3
	v_cvt_pk_bf16_f32 v3, v4, v5
	global_store_dwordx2 v[8:9], v[2:3], off offset:160
	v_pk_mul_f32 v[10:11], v[24:25], v[20:21] op_sel_hi:[1,0]
	v_pk_mul_f32 v[12:13], v[26:27], v[20:21] op_sel_hi:[1,0]
	v_pk_mul_f32 v[2:3], v[92:93], v[10:11]
	v_pk_mul_f32 v[4:5], v[94:95], v[12:13]
	v_cvt_pk_bf16_f32 v2, v2, v3
	v_cvt_pk_bf16_f32 v3, v4, v5
	global_store_dwordx2 v[8:9], v[2:3], off offset:192
	v_pk_mul_f32 v[10:11], v[22:23], v[20:21] op_sel_hi:[1,0]
	v_pk_mul_f32 v[2:3], v[96:97], v[6:7]
	v_pk_mul_f32 v[4:5], v[98:99], v[10:11]
	v_cvt_pk_bf16_f32 v2, v2, v3
	v_cvt_pk_bf16_f32 v3, v4, v5
	global_store_dwordx2 v[8:9], v[2:3], off offset:224
	s_cbranch_vccnz .LBB0_831

.LBB0_1882:
	ds_bpermute_b32 v1, v201, v220
	s_mov_b32 s68, 1
	s_mov_b64 s[30:31], 0
	s_waitcnt lgkmcnt(0)
	v_add_f32_e32 v1, v220, v1
	ds_bpermute_b32 v2, v202, v1
	s_waitcnt lgkmcnt(0)
	v_add_f32_e32 v1, v1, v2
	v_div_scale_f32 v2, s[0:1], v1, v1, 1.0
	v_rcp_f32_e32 v3, v2
	v_div_scale_f32 v4, vcc, 1.0, v1, 1.0
	v_fma_f32 v5, -v2, v3, 1.0
	v_fmac_f32_e32 v3, v5, v3
	v_mul_f32_e32 v5, v4, v3
	v_fma_f32 v6, -v2, v5, v4
	v_fmac_f32_e32 v5, v6, v3
	v_fma_f32 v2, -v2, v5, v4
	v_div_fmas_f32 v2, v2, v3, v5
	v_div_fixup_f32 v6, v2, v1, 1.0
	v_pk_mul_f32 v[10:11], v[80:81], v[6:7] op_sel_hi:[1,0]
	v_pk_mul_f32 v[14:15], v[76:77], v[6:7] op_sel_hi:[1,0]
	v_mov_b32_e32 v4, v11
	v_mov_b32_e32 v5, v15
	v_pk_mul_f32 v[8:9], v[82:83], v[6:7] op_sel_hi:[1,0]
	v_pk_mul_f32 v[12:13], v[78:79], v[6:7] op_sel_hi:[1,0]
	v_mov_b32_e32 v2, v10
	v_mov_b32_e32 v3, v14
	v_pk_mul_f32 v[4:5], v[4:5], v[4:5]
	v_mov_b32_e32 v16, v8
	v_pk_fma_f32 v[2:3], v[2:3], v[2:3], v[4:5]
	v_mov_b32_e32 v4, v9
	v_mov_b32_e32 v5, v13
	v_mov_b32_e32 v17, v12
	v_pk_mul_f32 v[4:5], v[4:5], v[4:5]
	v_pk_mul_f32 v[18:19], v[74:75], v[6:7] op_sel_hi:[1,0]
	v_pk_fma_f32 v[4:5], v[16:17], v[16:17], v[4:5]
	v_pk_mul_f32 v[16:17], v[72:73], v[6:7] op_sel_hi:[1,0]
	v_pk_add_f32 v[2:3], v[2:3], v[4:5]
	v_pk_mul_f32 v[4:5], v[18:19], v[18:19]
	s_waitcnt vmcnt(3)
	v_pk_mul_f32 v[28:29], v[16:17], v[16:17]
	v_pk_add_f32 v[2:3], v[2:3], v[2:3] op_sel_hi:[0,1]
	v_pk_mov_b32 v[30:31], v[28:29], v[4:5] op_sel:[1,0]
	v_mov_b32_e32 v29, v5
	v_pk_add_f32 v[4:5], v[30:31], v[28:29]
	v_pk_mul_f32 v[30:31], v[68:69], v[6:7] op_sel_hi:[1,0]
	v_pk_mul_f32 v[28:29], v[70:71], v[6:7] op_sel_hi:[1,0]
	v_mul_f32_e32 v2, v30, v30
	s_waitcnt vmcnt(2)
	v_pk_fma_f32 v[36:37], v[30:31], v[30:31], v[2:3] op_sel_hi:[1,1,0]
	v_mul_f32_e32 v2, v28, v28
	v_pk_add_f32 v[4:5], v[4:5], v[4:5] op_sel_hi:[0,1]
	v_pk_fma_f32 v[38:39], v[28:29], v[28:29], v[2:3] op_sel_hi:[1,1,0]
	s_waitcnt vmcnt(1)
	v_pk_mul_f32 v[40:41], v[66:67], v[6:7] op_sel_hi:[1,0]
	v_pk_mul_f32 v[42:43], v[64:65], v[6:7] op_sel_hi:[1,0]
	v_mul_f32_e32 v4, v40, v40
	v_mul_f32_e32 v36, v42, v42
	v_mul_f32_e32 v38, v43, v43
	v_mul_f32_e32 v2, v41, v41
	v_pk_add_f32 v[36:37], v[36:37], v[38:39]
	v_pk_add_f32 v[2:3], v[4:5], v[2:3]
	v_pk_mul_f32 v[32:33], v[32:33], v[6:7] op_sel_hi:[1,0]
	v_pk_add_f32 v[36:37], v[36:37], v[2:3]
	global_load_dwordx4 v[48:51], v[106:107], off
	global_load_dwordx4 v[52:55], v[106:107], off offset:64
	global_load_dwordx4 v[56:59], v[106:107], off offset:128
	global_load_dwordx4 v[60:63], v[106:107], off offset:192
	global_load_dwordx4 v[84:87], v[106:107], off offset:256
	global_load_dwordx4 v[88:91], v[106:107], off offset:320
	global_load_dwordx4 v[92:95], v[106:107], off offset:384
	global_load_dwordx4 v[96:99], v[106:107], off offset:448
	v_pk_mul_f32 v[34:35], v[34:35], v[6:7] op_sel_hi:[1,0]
	v_pk_add_f32 v[36:37], v[36:37], v[36:37] op_sel_hi:[0,1]
	v_pk_mul_f32 v[38:39], v[34:35], v[34:35]
	v_pk_mul_f32 v[44:45], v[32:33], v[32:33]
	v_pk_mul_f32 v[24:25], v[24:25], v[6:7] op_sel_hi:[1,0]
	v_pk_mov_b32 v[46:47], v[44:45], v[38:39] op_sel:[1,0]
	v_mov_b32_e32 v45, v39
	v_pk_mul_f32 v[26:27], v[26:27], v[6:7] op_sel_hi:[1,0]
	v_mul_f32_e32 v36, v24, v24
	v_pk_add_f32 v[38:39], v[46:47], v[44:45]
	v_pk_fma_f32 v[44:45], v[24:25], v[24:25], v[36:37] op_sel_hi:[1,1,0]
	v_mul_f32_e32 v36, v26, v26
	v_pk_add_f32 v[38:39], v[38:39], v[38:39] op_sel_hi:[0,1]
	v_pk_fma_f32 v[46:47], v[26:27], v[26:27], v[36:37] op_sel_hi:[1,1,0]
	v_pk_mul_f32 v[22:23], v[22:23], v[6:7] op_sel_hi:[1,0]
	v_pk_mul_f32 v[6:7], v[20:21], v[6:7] op_sel_hi:[1,0]
	v_mul_f32_e32 v38, v22, v22
	v_mul_f32_e32 v44, v6, v6
	v_mul_f32_e32 v46, v7, v7
	v_mul_f32_e32 v36, v23, v23
	v_pk_add_f32 v[20:21], v[44:45], v[46:47]
	v_pk_add_f32 v[36:37], v[38:39], v[36:37]
	s_nop 0
	v_pk_add_f32 v[20:21], v[20:21], v[36:37]
	s_nop 0
	v_add_f32_e32 v1, v20, v21
	ds_bpermute_b32 v20, v201, v1
	s_waitcnt lgkmcnt(0)
	v_add_f32_e32 v1, v1, v20
	ds_bpermute_b32 v20, v202, v1
	s_waitcnt lgkmcnt(0)
	v_add_f32_e32 v1, v1, v20
	v_fmamk_f32 v1, v1, 0x3c000000, v209
	v_mul_f32_e32 v20, 0x4f800000, v1
	v_cmp_gt_f32_e32 vcc, s62, v1
	s_nop 1
	v_cndmask_b32_e32 v1, v1, v20, vcc
	v_sqrt_f32_e32 v20, v1
	s_nop 0
	v_add_u32_e32 v21, -1, v20
	v_fma_f32 v36, -v21, v20, v1
	v_cmp_ge_f32_e64 s[6:7], 0, v36
	v_add_u32_e32 v36, 1, v20
	s_nop 0
	v_cndmask_b32_e64 v21, v20, v21, s[6:7]
	v_fma_f32 v20, -v36, v20, v1
	v_cmp_lt_f32_e64 s[6:7], 0, v20
	s_nop 1
	v_cndmask_b32_e64 v20, v21, v36, s[6:7]
	v_mul_f32_e32 v21, 0x37800000, v20
	v_cndmask_b32_e32 v20, v20, v21, vcc
	v_cmp_class_f32_e32 vcc, v1, v210
	s_nop 1
	v_cndmask_b32_e32 v1, v20, v1, vcc
	v_div_scale_f32 v20, s[0:1], v1, v1, 1.0
	v_rcp_f32_e32 v21, v20
	s_nop 0
	v_fma_f32 v36, -v20, v21, 1.0
	v_fmac_f32_e32 v21, v36, v21
	v_div_scale_f32 v36, vcc, 1.0, v1, 1.0
	v_mul_f32_e32 v37, v36, v21
	v_fma_f32 v38, -v20, v37, v36
	v_fmac_f32_e32 v37, v38, v21
	v_fma_f32 v20, -v20, v37, v36
	v_div_fmas_f32 v20, v20, v21, v37
	v_lshlrev_b64 v[36:37], 12, v[152:153]
	v_div_fixup_f32 v20, v20, v1, 1.0
	v_lshl_add_u64 v[36:37], s[16:17], 0, v[36:37]
	v_lshl_add_u64 v[36:37], v[36:37], 0, s[4:5]
	v_pk_mul_f32 v[10:11], v[10:11], v[20:21] op_sel_hi:[1,0]
	v_pk_mul_f32 v[8:9], v[8:9], v[20:21] op_sel_hi:[1,0]
	v_lshl_add_u64 v[36:37], v[104:105], 1, v[36:37]
	s_waitcnt vmcnt(0)
	v_pk_mul_f32 v[2:3], v[48:49], v[10:11]
	v_pk_mul_f32 v[4:5], v[50:51], v[8:9]
	v_cvt_pk_bf16_f32 v2, v2, v3
	v_cvt_pk_bf16_f32 v3, v4, v5
	v_add_co_u32_e32 v4, vcc, s63, v36
	v_pk_mul_f32 v[10:11], v[14:15], v[20:21] op_sel_hi:[1,0]
	s_nop 0
	v_addc_co_u32_e32 v5, vcc, 0, v37, vcc
	global_store_dwordx2 v[4:5], v[2:3], off offset:2048
	v_pk_mul_f32 v[12:13], v[12:13], v[20:21] op_sel_hi:[1,0]
	v_lshl_add_u64 v[8:9], v[36:37], 0, s[28:29]
	v_pk_mul_f32 v[6:7], v[6:7], v[20:21] op_sel_hi:[1,0]
	s_and_b64 vcc, exec, s[8:9]
	v_pk_mul_f32 v[2:3], v[52:53], v[10:11]
	v_pk_mul_f32 v[4:5], v[54:55], v[12:13]
	v_cvt_pk_bf16_f32 v2, v2, v3
	v_cvt_pk_bf16_f32 v3, v4, v5
	global_store_dwordx2 v[8:9], v[2:3], off offset:32
	v_pk_mul_f32 v[10:11], v[16:17], v[20:21] op_sel_hi:[1,0]
	v_pk_mul_f32 v[12:13], v[18:19], v[20:21] op_sel_hi:[1,0]
	v_pk_mul_f32 v[2:3], v[56:57], v[10:11]
	v_pk_mul_f32 v[4:5], v[58:59], v[12:13]
	v_cvt_pk_bf16_f32 v2, v2, v3
	v_cvt_pk_bf16_f32 v3, v4, v5
	global_store_dwordx2 v[8:9], v[2:3], off offset:64
	v_pk_mul_f32 v[10:11], v[30:31], v[20:21] op_sel_hi:[1,0]
	v_pk_mul_f32 v[12:13], v[28:29], v[20:21] op_sel_hi:[1,0]
	v_pk_mul_f32 v[2:3], v[60:61], v[10:11]
	v_pk_mul_f32 v[4:5], v[62:63], v[12:13]
	v_cvt_pk_bf16_f32 v2, v2, v3
	v_cvt_pk_bf16_f32 v3, v4, v5
	global_store_dwordx2 v[8:9], v[2:3], off offset:96
	v_pk_mul_f32 v[10:11], v[42:43], v[20:21] op_sel_hi:[1,0]
	v_pk_mul_f32 v[12:13], v[40:41], v[20:21] op_sel_hi:[1,0]
	v_pk_mul_f32 v[2:3], v[84:85], v[10:11]
	v_pk_mul_f32 v[4:5], v[86:87], v[12:13]
	v_cvt_pk_bf16_f32 v2, v2, v3
	v_cvt_pk_bf16_f32 v3, v4, v5
	global_store_dwordx2 v[8:9], v[2:3], off offset:128
	v_pk_mul_f32 v[10:11], v[32:33], v[20:21] op_sel_hi:[1,0]
	v_pk_mul_f32 v[12:13], v[34:35], v[20:21] op_sel_hi:[1,0]
	v_pk_mul_f32 v[2:3], v[88:89], v[10:11]
	v_pk_mul_f32 v[4:5], v[90:91], v[12:13]
	v_cvt_pk_bf16_f32 v2, v2, v3
	v_cvt_pk_bf16_f32 v3, v4, v5
	global_store_dwordx2 v[8:9], v[2:3], off offset:160
	v_pk_mul_f32 v[10:11], v[24:25], v[20:21] op_sel_hi:[1,0]
	v_pk_mul_f32 v[12:13], v[26:27], v[20:21] op_sel_hi:[1,0]
	v_pk_mul_f32 v[2:3], v[92:93], v[10:11]
	v_pk_mul_f32 v[4:5], v[94:95], v[12:13]
	v_cvt_pk_bf16_f32 v2, v2, v3
	v_cvt_pk_bf16_f32 v3, v4, v5
	global_store_dwordx2 v[8:9], v[2:3], off offset:192
	v_pk_mul_f32 v[10:11], v[22:23], v[20:21] op_sel_hi:[1,0]
	v_pk_mul_f32 v[2:3], v[96:97], v[6:7]
	v_pk_mul_f32 v[4:5], v[98:99], v[10:11]
	v_cvt_pk_bf16_f32 v2, v2, v3
	v_cvt_pk_bf16_f32 v3, v4, v5
	global_store_dwordx2 v[8:9], v[2:3], off offset:224
	s_cbranch_vccnz .LBB0_1925
